# MoE gate/up epilogue rewritten: packed f32 silu math, slot/gate loads overlapped with math, 32-bit offset addressing, stores after all math
# baseline (speedup 1.0000x reference)
;     __device__ __forceinline__ void operator()(const f32x4 (&acc)[2][2][4][2], const Unit& u, int wr, int wc, int fr, int fq) const {
;     ...
;         int slots[8]; float scv[8], gwv[8];
; #pragma unroll
;         for (int j = 0; j < 8; ++j) { const int r = (j >> 2) * HALF + wr * 64 + (j & 3) * 16 + fr; slots[j] = list[u.e * LCAP + u.pm * BM + (r < u.rows ? r : u.rows - 1)]; }
; #pragma unroll
;         for (int j = 0; j < 8; ++j) { scv[j] = rsc ? rsc[slots[j]] * cs : cs; gwv[j] = gatew[slots[j]]; }
; #pragma unroll
;         for (int ai = 0; ai < 2; ++ai)
; #pragma unroll
;             for (int m = 0; m < 4; ++m) {
;                 const int r = ai * HALF + wr * 64 + m * 16 + fr; const bool valid = r < u.rows;
;                 const int slot = slots[ai * 4 + m];
;                 const float sc = scv[ai * 4 + m], gw = gwv[ai * 4 + m]; float o[8];
; #pragma unroll
;                 for (int n = 0; n < 2; ++n) { const f32x4 g = acc[ai][0][m][n] * sc, up = acc[ai][1][m][n] * sc;
; #pragma unroll
;                     for (int j = 0; j < 4; ++j) o[4 * n + j] = g[j] * __builtin_amdgcn_rcpf(1.0f + __expf(-g[j])) * up[j] * gw; }
.LBB0_1605:
	v_mbcnt_lo_u32_b32 v64, -1, 0
	v_mbcnt_hi_u32_b32 v64, -1, v64
	s_lshl_b32 s0, s6, 14
	s_lshl_b32 s1, s33, 8
	v_add_u32_e32 v153, s93, v64
	s_add_i32 s0, s0, s1
	s_add_i32 s1, s40, -1
	v_and_b32_e32 v64, 15, v153
	v_bfe_u32 v155, v153, 4, 2
	v_or_b32_e32 v156, s49, v64
	s_lshl_b32 s23, s28, 7
	v_min_i32_e32 v152, s1, v156
	v_add_lshl_u32 v152, v152, s0, 2
	global_load_dword v130, v152, s[12:13]
	v_add_u32_e32 v152, 16, v156
	v_min_i32_e32 v152, s1, v152
	v_add_lshl_u32 v152, v152, s0, 2
	global_load_dword v131, v152, s[12:13]
	v_add_u32_e32 v152, 32, v156
	v_min_i32_e32 v152, s1, v152
	v_add_lshl_u32 v152, v152, s0, 2
	global_load_dword v132, v152, s[12:13]
	v_add_u32_e32 v152, 48, v156
	v_min_i32_e32 v152, s1, v152
	v_add_lshl_u32 v152, v152, s0, 2
	global_load_dword v133, v152, s[12:13]
	v_add_u32_e32 v152, 0x80, v156
	v_min_i32_e32 v152, s1, v152
	v_add_lshl_u32 v152, v152, s0, 2
	global_load_dword v134, v152, s[12:13]
	v_add_u32_e32 v152, 0x90, v156
	v_min_i32_e32 v152, s1, v152
	v_add_lshl_u32 v152, v152, s0, 2
	global_load_dword v135, v152, s[12:13]
	v_add_u32_e32 v152, 0xa0, v156
	v_min_i32_e32 v152, s1, v152
	v_add_lshl_u32 v152, v152, s0, 2
	global_load_dword v136, v152, s[12:13]
	v_add_u32_e32 v152, 0xb0, v156
	v_min_i32_e32 v152, s1, v152
	v_add_lshl_u32 v152, v152, s0, 2
	global_load_dword v137, v152, s[12:13]
	v_mov_b32_e32 v66, 0xbcb8aa3b
	v_mov_b32_e32 v67, 0xbcb8aa3b
	v_mov_b32_e32 v68, 1.0
	v_mov_b32_e32 v69, 1.0
	v_lshl_or_b32 v166, v155, 3, s23
	v_or_b32_e32 v166, s50, v166
	v_lshlrev_b32_e32 v166, 1, v166
	v_mov_b32_e32 v218, 0x358637bd
	v_mov_b32_e32 v219, 0x43e00000
	v_mov_b32_e32 v226, 0xff800000
	v_mov_b64_e32 v[228:229], 0x1e8481
	v_pk_mul_f32 v[158:159], v[126:127], v[66:67]
	v_pk_mul_f32 v[160:161], v[128:129], v[66:67]
	v_pk_mul_f32 v[162:163], v[118:119], v[66:67]
	v_pk_mul_f32 v[164:165], v[120:121], v[66:67]
	v_exp_f32_e32 v158, v158
	v_exp_f32_e32 v159, v159
	v_exp_f32_e32 v160, v160
	v_exp_f32_e32 v161, v161
	v_exp_f32_e32 v162, v162
	v_exp_f32_e32 v163, v163
	v_exp_f32_e32 v164, v164
	v_exp_f32_e32 v165, v165
	v_pk_add_f32 v[158:159], v[158:159], v[68:69]
	v_pk_add_f32 v[160:161], v[160:161], v[68:69]
	v_pk_add_f32 v[162:163], v[162:163], v[68:69]
	v_pk_add_f32 v[164:165], v[164:165], v[68:69]
	v_pk_mul_f32 v[122:123], v[126:127], v[122:123]
	v_pk_mul_f32 v[124:125], v[128:129], v[124:125]
	v_pk_mul_f32 v[114:115], v[118:119], v[114:115]
	v_pk_mul_f32 v[116:117], v[120:121], v[116:117]
	v_rcp_f32_e32 v158, v158
	v_rcp_f32_e32 v159, v159
	v_rcp_f32_e32 v160, v160
	v_rcp_f32_e32 v161, v161
	v_rcp_f32_e32 v162, v162
	v_rcp_f32_e32 v163, v163
	v_rcp_f32_e32 v164, v164
	v_rcp_f32_e32 v165, v165
	v_pk_mul_f32 v[122:123], v[122:123], v[158:159]
	v_pk_mul_f32 v[124:125], v[124:125], v[160:161]
	v_pk_mul_f32 v[114:115], v[114:115], v[162:163]
	v_pk_mul_f32 v[116:117], v[116:117], v[164:165]
	v_pk_mul_f32 v[158:159], v[110:111], v[66:67]
	v_pk_mul_f32 v[160:161], v[112:113], v[66:67]
	v_pk_mul_f32 v[162:163], v[102:103], v[66:67]
	v_pk_mul_f32 v[164:165], v[104:105], v[66:67]
	v_exp_f32_e32 v158, v158
	v_exp_f32_e32 v159, v159
	v_exp_f32_e32 v160, v160
	v_exp_f32_e32 v161, v161
	v_exp_f32_e32 v162, v162
	v_exp_f32_e32 v163, v163
	v_exp_f32_e32 v164, v164
	v_exp_f32_e32 v165, v165
	v_pk_add_f32 v[158:159], v[158:159], v[68:69]
	v_pk_add_f32 v[160:161], v[160:161], v[68:69]
	v_pk_add_f32 v[162:163], v[162:163], v[68:69]
	v_pk_add_f32 v[164:165], v[164:165], v[68:69]
	v_pk_mul_f32 v[106:107], v[110:111], v[106:107]
	v_pk_mul_f32 v[108:109], v[112:113], v[108:109]
	v_pk_mul_f32 v[98:99], v[102:103], v[98:99]
	v_pk_mul_f32 v[100:101], v[104:105], v[100:101]
	v_rcp_f32_e32 v158, v158
	v_rcp_f32_e32 v159, v159
	v_rcp_f32_e32 v160, v160
	v_rcp_f32_e32 v161, v161
	v_rcp_f32_e32 v162, v162
	v_rcp_f32_e32 v163, v163
	v_rcp_f32_e32 v164, v164
	v_rcp_f32_e32 v165, v165
	v_pk_mul_f32 v[106:107], v[106:107], v[158:159]
	v_pk_mul_f32 v[108:109], v[108:109], v[160:161]
	v_pk_mul_f32 v[98:99], v[98:99], v[162:163]
	v_pk_mul_f32 v[100:101], v[100:101], v[164:165]
	v_pk_mul_f32 v[158:159], v[94:95], v[66:67]
	v_pk_mul_f32 v[160:161], v[96:97], v[66:67]
	v_pk_mul_f32 v[162:163], v[86:87], v[66:67]
	v_pk_mul_f32 v[164:165], v[88:89], v[66:67]
	v_exp_f32_e32 v158, v158
	v_exp_f32_e32 v159, v159
	v_exp_f32_e32 v160, v160
	v_exp_f32_e32 v161, v161
	v_exp_f32_e32 v162, v162
	v_exp_f32_e32 v163, v163
	v_exp_f32_e32 v164, v164
	v_exp_f32_e32 v165, v165
	v_pk_add_f32 v[158:159], v[158:159], v[68:69]
	v_pk_add_f32 v[160:161], v[160:161], v[68:69]
	v_pk_add_f32 v[162:163], v[162:163], v[68:69]
	v_pk_add_f32 v[164:165], v[164:165], v[68:69]
	v_pk_mul_f32 v[90:91], v[94:95], v[90:91]
	v_pk_mul_f32 v[92:93], v[96:97], v[92:93]
	v_pk_mul_f32 v[82:83], v[86:87], v[82:83]
	v_pk_mul_f32 v[84:85], v[88:89], v[84:85]
	v_rcp_f32_e32 v158, v158
	v_rcp_f32_e32 v159, v159
	v_rcp_f32_e32 v160, v160
	v_rcp_f32_e32 v161, v161
	v_rcp_f32_e32 v162, v162
	v_rcp_f32_e32 v163, v163
	v_rcp_f32_e32 v164, v164
	v_rcp_f32_e32 v165, v165
	v_pk_mul_f32 v[90:91], v[90:91], v[158:159]
	v_pk_mul_f32 v[92:93], v[92:93], v[160:161]
	v_pk_mul_f32 v[82:83], v[82:83], v[162:163]
	v_pk_mul_f32 v[84:85], v[84:85], v[164:165]
	v_pk_mul_f32 v[158:159], v[78:79], v[66:67]
	v_pk_mul_f32 v[160:161], v[80:81], v[66:67]
	v_pk_mul_f32 v[162:163], v[70:71], v[66:67]
	v_pk_mul_f32 v[164:165], v[72:73], v[66:67]
	v_exp_f32_e32 v158, v158
	v_exp_f32_e32 v159, v159
	v_exp_f32_e32 v160, v160
	v_exp_f32_e32 v161, v161
	v_exp_f32_e32 v162, v162
	v_exp_f32_e32 v163, v163
	v_exp_f32_e32 v164, v164
	v_exp_f32_e32 v165, v165
	v_pk_add_f32 v[158:159], v[158:159], v[68:69]
	v_pk_add_f32 v[160:161], v[160:161], v[68:69]
	v_pk_add_f32 v[162:163], v[162:163], v[68:69]
	v_pk_add_f32 v[164:165], v[164:165], v[68:69]
	v_pk_mul_f32 v[74:75], v[78:79], v[74:75]
	v_pk_mul_f32 v[76:77], v[80:81], v[76:77]
	v_pk_mul_f32 v[12:13], v[70:71], v[12:13]
	v_pk_mul_f32 v[14:15], v[72:73], v[14:15]
	v_rcp_f32_e32 v158, v158
	v_rcp_f32_e32 v159, v159
	v_rcp_f32_e32 v160, v160
	v_rcp_f32_e32 v161, v161
	v_rcp_f32_e32 v162, v162
	v_rcp_f32_e32 v163, v163
	v_rcp_f32_e32 v164, v164
	v_rcp_f32_e32 v165, v165
	v_pk_mul_f32 v[74:75], v[74:75], v[158:159]
	v_pk_mul_f32 v[76:77], v[76:77], v[160:161]
	v_pk_mul_f32 v[12:13], v[12:13], v[162:163]
	v_pk_mul_f32 v[14:15], v[14:15], v[164:165]
	s_waitcnt vmcnt(0)
;     __device__ __forceinline__ void operator()(const f32x4 (&acc)[2][2][4][2], const Unit& u, int wr, int wc, int fr, int fq) const {
;     ...
;         for (int j = 0; j < 8; ++j) { scv[j] = rsc ? rsc[slots[j]] * cs : cs; gwv[j] = gatew[slots[j]]; }
;     ...
;                 for (int n = 0; n < 2; ++n) { const f32x4 g = acc[ai][0][m][n] * sc, up = acc[ai][1][m][n] * sc;
; #pragma unroll
;                     for (int j = 0; j < 4; ++j) o[4 * n + j] = g[j] * __builtin_amdgcn_rcpf(1.0f + __expf(-g[j])) * up[j] * gw; }
	v_lshlrev_b32_e32 v152, 2, v130
	global_load_dword v138, v152, s[16:17]
	v_lshlrev_b32_e32 v152, 2, v131
	global_load_dword v139, v152, s[16:17]
	v_lshlrev_b32_e32 v152, 2, v132
	global_load_dword v140, v152, s[16:17]
	v_lshlrev_b32_e32 v152, 2, v133
	global_load_dword v141, v152, s[16:17]
	v_lshlrev_b32_e32 v152, 2, v134
	global_load_dword v142, v152, s[16:17]
	v_lshlrev_b32_e32 v152, 2, v135
	global_load_dword v143, v152, s[16:17]
	v_lshlrev_b32_e32 v152, 2, v136
	global_load_dword v144, v152, s[16:17]
	v_lshlrev_b32_e32 v152, 2, v137
	global_load_dword v145, v152, s[16:17]
	v_pk_mul_f32 v[158:159], v[60:61], v[66:67]
	v_pk_mul_f32 v[160:161], v[62:63], v[66:67]
	v_pk_mul_f32 v[162:163], v[52:53], v[66:67]
	v_pk_mul_f32 v[164:165], v[54:55], v[66:67]
	v_exp_f32_e32 v158, v158
	v_exp_f32_e32 v159, v159
	v_exp_f32_e32 v160, v160
	v_exp_f32_e32 v161, v161
	v_exp_f32_e32 v162, v162
	v_exp_f32_e32 v163, v163
	v_exp_f32_e32 v164, v164
	v_exp_f32_e32 v165, v165
	v_pk_add_f32 v[158:159], v[158:159], v[68:69]
	v_pk_add_f32 v[160:161], v[160:161], v[68:69]
	v_pk_add_f32 v[162:163], v[162:163], v[68:69]
	v_pk_add_f32 v[164:165], v[164:165], v[68:69]
	v_pk_mul_f32 v[56:57], v[60:61], v[56:57]
	v_pk_mul_f32 v[58:59], v[62:63], v[58:59]
	v_pk_mul_f32 v[48:49], v[52:53], v[48:49]
	v_pk_mul_f32 v[50:51], v[54:55], v[50:51]
	v_rcp_f32_e32 v158, v158
	v_rcp_f32_e32 v159, v159
	v_rcp_f32_e32 v160, v160
	v_rcp_f32_e32 v161, v161
	v_rcp_f32_e32 v162, v162
	v_rcp_f32_e32 v163, v163
	v_rcp_f32_e32 v164, v164
	v_rcp_f32_e32 v165, v165
	v_pk_mul_f32 v[56:57], v[56:57], v[158:159]
	v_pk_mul_f32 v[58:59], v[58:59], v[160:161]
	v_pk_mul_f32 v[48:49], v[48:49], v[162:163]
	v_pk_mul_f32 v[50:51], v[50:51], v[164:165]
	v_pk_mul_f32 v[158:159], v[44:45], v[66:67]
	v_pk_mul_f32 v[160:161], v[46:47], v[66:67]
	v_pk_mul_f32 v[162:163], v[36:37], v[66:67]
	v_pk_mul_f32 v[164:165], v[38:39], v[66:67]
	v_exp_f32_e32 v158, v158
	v_exp_f32_e32 v159, v159
	v_exp_f32_e32 v160, v160
	v_exp_f32_e32 v161, v161
	v_exp_f32_e32 v162, v162
	v_exp_f32_e32 v163, v163
	v_exp_f32_e32 v164, v164
	v_exp_f32_e32 v165, v165
	v_pk_add_f32 v[158:159], v[158:159], v[68:69]
	v_pk_add_f32 v[160:161], v[160:161], v[68:69]
	v_pk_add_f32 v[162:163], v[162:163], v[68:69]
	v_pk_add_f32 v[164:165], v[164:165], v[68:69]
	v_pk_mul_f32 v[40:41], v[44:45], v[40:41]
	v_pk_mul_f32 v[42:43], v[46:47], v[42:43]
	v_pk_mul_f32 v[32:33], v[36:37], v[32:33]
	v_pk_mul_f32 v[34:35], v[38:39], v[34:35]
	v_rcp_f32_e32 v158, v158
	v_rcp_f32_e32 v159, v159
	v_rcp_f32_e32 v160, v160
	v_rcp_f32_e32 v161, v161
	v_rcp_f32_e32 v162, v162
	v_rcp_f32_e32 v163, v163
	v_rcp_f32_e32 v164, v164
	v_rcp_f32_e32 v165, v165
	v_pk_mul_f32 v[40:41], v[40:41], v[158:159]
	v_pk_mul_f32 v[42:43], v[42:43], v[160:161]
	v_pk_mul_f32 v[32:33], v[32:33], v[162:163]
	v_pk_mul_f32 v[34:35], v[34:35], v[164:165]
	v_pk_mul_f32 v[158:159], v[24:25], v[66:67]
	v_pk_mul_f32 v[160:161], v[26:27], v[66:67]
	v_pk_mul_f32 v[162:163], v[16:17], v[66:67]
	v_pk_mul_f32 v[164:165], v[18:19], v[66:67]
	v_exp_f32_e32 v158, v158
	v_exp_f32_e32 v159, v159
	v_exp_f32_e32 v160, v160
	v_exp_f32_e32 v161, v161
	v_exp_f32_e32 v162, v162
	v_exp_f32_e32 v163, v163
	v_exp_f32_e32 v164, v164
	v_exp_f32_e32 v165, v165
	v_pk_add_f32 v[158:159], v[158:159], v[68:69]
	v_pk_add_f32 v[160:161], v[160:161], v[68:69]
	v_pk_add_f32 v[162:163], v[162:163], v[68:69]
	v_pk_add_f32 v[164:165], v[164:165], v[68:69]
	v_pk_mul_f32 v[28:29], v[24:25], v[28:29]
	v_pk_mul_f32 v[30:31], v[26:27], v[30:31]
	v_pk_mul_f32 v[20:21], v[16:17], v[20:21]
	v_pk_mul_f32 v[22:23], v[18:19], v[22:23]
	v_rcp_f32_e32 v158, v158
	v_rcp_f32_e32 v159, v159
	v_rcp_f32_e32 v160, v160
	v_rcp_f32_e32 v161, v161
	v_rcp_f32_e32 v162, v162
	v_rcp_f32_e32 v163, v163
	v_rcp_f32_e32 v164, v164
	v_rcp_f32_e32 v165, v165
	v_pk_mul_f32 v[28:29], v[28:29], v[158:159]
	v_pk_mul_f32 v[30:31], v[30:31], v[160:161]
	v_pk_mul_f32 v[20:21], v[20:21], v[162:163]
	v_pk_mul_f32 v[22:23], v[22:23], v[164:165]
	v_pk_mul_f32 v[158:159], v[8:9], v[66:67]
	v_pk_mul_f32 v[160:161], v[10:11], v[66:67]
	v_pk_mul_f32 v[162:163], v[230:231], v[66:67]
	v_pk_mul_f32 v[164:165], v[232:233], v[66:67]
	v_exp_f32_e32 v158, v158
	v_exp_f32_e32 v159, v159
	v_exp_f32_e32 v160, v160
	v_exp_f32_e32 v161, v161
	v_exp_f32_e32 v162, v162
	v_exp_f32_e32 v163, v163
	v_exp_f32_e32 v164, v164
	v_exp_f32_e32 v165, v165
	v_pk_add_f32 v[158:159], v[158:159], v[68:69]
	v_pk_add_f32 v[160:161], v[160:161], v[68:69]
	v_pk_add_f32 v[162:163], v[162:163], v[68:69]
	v_pk_add_f32 v[164:165], v[164:165], v[68:69]
	v_pk_mul_f32 v[0:1], v[8:9], v[0:1]
	v_pk_mul_f32 v[2:3], v[10:11], v[2:3]
	v_pk_mul_f32 v[4:5], v[230:231], v[4:5]
	v_pk_mul_f32 v[6:7], v[232:233], v[6:7]
	v_rcp_f32_e32 v158, v158
	v_rcp_f32_e32 v159, v159
	v_rcp_f32_e32 v160, v160
	v_rcp_f32_e32 v161, v161
	v_rcp_f32_e32 v162, v162
	v_rcp_f32_e32 v163, v163
	v_rcp_f32_e32 v164, v164
	v_rcp_f32_e32 v165, v165
	v_pk_mul_f32 v[0:1], v[0:1], v[158:159]
	v_pk_mul_f32 v[2:3], v[2:3], v[160:161]
	v_pk_mul_f32 v[4:5], v[4:5], v[162:163]
	v_pk_mul_f32 v[6:7], v[6:7], v[164:165]
	s_waitcnt vmcnt(7)
; __device__ __forceinline__ unsigned cvt_pk_bf16(float lo, float hi) { unsigned r; asm volatile("v_cvt_pk_bf16_f32 %0, %1, %2" : "=v"(r) : "v"(lo), "v"(hi)); return r; }
; __device__ __forceinline__ void st_wt16(void* p, u32x4 v) { asm volatile("global_store_dwordx4 %0, %1, off sc1\n\ts_nop 1" :: "v"(p), "v"(v) : "memory"); }
;     __device__ __forceinline__ void operator()(const f32x4 (&acc)[2][2][4][2], const Unit& u, int wr, int wc, int fr, int fq) const {
;     ...
;                 const int r = ai * HALF + wr * 64 + m * 16 + fr; const bool valid = r < u.rows;
;                 const int slot = slots[ai * 4 + m];
;                 const float sc = scv[ai * 4 + m], gw = gwv[ai * 4 + m]; float o[8];
; #pragma unroll
;                 for (int n = 0; n < 2; ++n) { const f32x4 g = acc[ai][0][m][n] * sc, up = acc[ai][1][m][n] * sc;
; #pragma unroll
;                     for (int j = 0; j < 4; ++j) o[4 * n + j] = g[j] * __builtin_amdgcn_rcpf(1.0f + __expf(-g[j])) * up[j] * gw; }
;                 u32x4 w; w.x = cvt_pk_bf16(o[0], o[1]); w.y = cvt_pk_bf16(o[2], o[3]); w.z = cvt_pk_bf16(o[4], o[5]); w.w = cvt_pk_bf16(o[6], o[7]);
;                 if (valid) st_wt16(hid + (size_t)slot * 512 + f0, w);
;             }
;         wave_publish(ready + 64 * (moe[u.e] + u.pm), fr, fq);
	v_mul_f32_e32 v146, 0x39800000, v138
	v_lshl_add_u32 v152, v130, 10, v166
	v_mov_b32_e32 v147, v146
	v_pk_mul_f32 v[122:123], v[122:123], v[146:147]
	v_pk_mul_f32 v[124:125], v[124:125], v[146:147]
	v_pk_mul_f32 v[114:115], v[114:115], v[146:147]
	v_pk_mul_f32 v[116:117], v[116:117], v[146:147]
	v_cmp_gt_i32_e32 vcc, s40, v156
	v_cvt_pk_bf16_f32 v122, v122, v123
	v_cvt_pk_bf16_f32 v123, v124, v125
	v_cvt_pk_bf16_f32 v124, v114, v115
	v_cvt_pk_bf16_f32 v125, v116, v117
	s_and_saveexec_b64 s[0:1], vcc
	global_store_dwordx4 v152, v[122:125], s[10:11] sc1
	s_or_b64 exec, exec, s[0:1]
	s_waitcnt vmcnt(7)
	v_mul_f32_e32 v146, 0x39800000, v139
	v_lshl_add_u32 v152, v131, 10, v166
	v_mov_b32_e32 v147, v146
	v_add_u32_e32 v153, 16, v156
	v_pk_mul_f32 v[106:107], v[106:107], v[146:147]
	v_pk_mul_f32 v[108:109], v[108:109], v[146:147]
	v_pk_mul_f32 v[98:99], v[98:99], v[146:147]
	v_pk_mul_f32 v[100:101], v[100:101], v[146:147]
	v_cmp_gt_i32_e32 vcc, s40, v153
	v_cvt_pk_bf16_f32 v106, v106, v107
	v_cvt_pk_bf16_f32 v107, v108, v109
	v_cvt_pk_bf16_f32 v108, v98, v99
	v_cvt_pk_bf16_f32 v109, v100, v101
	s_and_saveexec_b64 s[0:1], vcc
	global_store_dwordx4 v152, v[106:109], s[10:11] sc1
	s_or_b64 exec, exec, s[0:1]
	s_waitcnt vmcnt(7)
	v_mul_f32_e32 v146, 0x39800000, v140
	v_lshl_add_u32 v152, v132, 10, v166
	v_mov_b32_e32 v147, v146
	v_add_u32_e32 v153, 32, v156
	v_pk_mul_f32 v[90:91], v[90:91], v[146:147]
	v_pk_mul_f32 v[92:93], v[92:93], v[146:147]
	v_pk_mul_f32 v[82:83], v[82:83], v[146:147]
	v_pk_mul_f32 v[84:85], v[84:85], v[146:147]
	v_cmp_gt_i32_e32 vcc, s40, v153
	v_cvt_pk_bf16_f32 v90, v90, v91
	v_cvt_pk_bf16_f32 v91, v92, v93
	v_cvt_pk_bf16_f32 v92, v82, v83
	v_cvt_pk_bf16_f32 v93, v84, v85
	s_and_saveexec_b64 s[0:1], vcc
	global_store_dwordx4 v152, v[90:93], s[10:11] sc1
	s_or_b64 exec, exec, s[0:1]
	s_waitcnt vmcnt(7)
	v_mul_f32_e32 v146, 0x39800000, v141
	v_lshl_add_u32 v152, v133, 10, v166
	v_mov_b32_e32 v147, v146
	v_add_u32_e32 v153, 48, v156
	v_pk_mul_f32 v[74:75], v[74:75], v[146:147]
	v_pk_mul_f32 v[76:77], v[76:77], v[146:147]
	v_pk_mul_f32 v[12:13], v[12:13], v[146:147]
	v_pk_mul_f32 v[14:15], v[14:15], v[146:147]
	v_cmp_gt_i32_e32 vcc, s40, v153
	v_cvt_pk_bf16_f32 v74, v74, v75
	v_cvt_pk_bf16_f32 v75, v76, v77
	v_cvt_pk_bf16_f32 v76, v12, v13
	v_cvt_pk_bf16_f32 v77, v14, v15
	s_and_saveexec_b64 s[0:1], vcc
	global_store_dwordx4 v152, v[74:77], s[10:11] sc1
	s_or_b64 exec, exec, s[0:1]
	s_waitcnt vmcnt(7)
	v_mul_f32_e32 v146, 0x39800000, v142
	v_lshl_add_u32 v152, v134, 10, v166
	v_mov_b32_e32 v147, v146
	v_add_u32_e32 v153, 0x80, v156
	v_pk_mul_f32 v[56:57], v[56:57], v[146:147]
	v_pk_mul_f32 v[58:59], v[58:59], v[146:147]
	v_pk_mul_f32 v[48:49], v[48:49], v[146:147]
	v_pk_mul_f32 v[50:51], v[50:51], v[146:147]
	v_cmp_gt_i32_e32 vcc, s40, v153
	v_cvt_pk_bf16_f32 v56, v56, v57
	v_cvt_pk_bf16_f32 v57, v58, v59
	v_cvt_pk_bf16_f32 v58, v48, v49
	v_cvt_pk_bf16_f32 v59, v50, v51
	s_and_saveexec_b64 s[0:1], vcc
	global_store_dwordx4 v152, v[56:59], s[10:11] sc1
	s_or_b64 exec, exec, s[0:1]
	s_waitcnt vmcnt(7)
	v_mul_f32_e32 v146, 0x39800000, v143
	v_lshl_add_u32 v152, v135, 10, v166
	v_mov_b32_e32 v147, v146
	v_add_u32_e32 v153, 0x90, v156
	v_pk_mul_f32 v[40:41], v[40:41], v[146:147]
	v_pk_mul_f32 v[42:43], v[42:43], v[146:147]
	v_pk_mul_f32 v[32:33], v[32:33], v[146:147]
	v_pk_mul_f32 v[34:35], v[34:35], v[146:147]
	v_cmp_gt_i32_e32 vcc, s40, v153
	v_cvt_pk_bf16_f32 v40, v40, v41
	v_cvt_pk_bf16_f32 v41, v42, v43
	v_cvt_pk_bf16_f32 v42, v32, v33
	v_cvt_pk_bf16_f32 v43, v34, v35
	s_and_saveexec_b64 s[0:1], vcc
	global_store_dwordx4 v152, v[40:43], s[10:11] sc1
	s_or_b64 exec, exec, s[0:1]
	s_waitcnt vmcnt(7)
	v_mul_f32_e32 v146, 0x39800000, v144
	v_lshl_add_u32 v152, v136, 10, v166
	v_mov_b32_e32 v147, v146
	v_add_u32_e32 v153, 0xa0, v156
	v_pk_mul_f32 v[28:29], v[28:29], v[146:147]
	v_pk_mul_f32 v[30:31], v[30:31], v[146:147]
	v_pk_mul_f32 v[20:21], v[20:21], v[146:147]
	v_pk_mul_f32 v[22:23], v[22:23], v[146:147]
	v_cmp_gt_i32_e32 vcc, s40, v153
	v_cvt_pk_bf16_f32 v28, v28, v29
	v_cvt_pk_bf16_f32 v29, v30, v31
	v_cvt_pk_bf16_f32 v30, v20, v21
	v_cvt_pk_bf16_f32 v31, v22, v23
	s_and_saveexec_b64 s[0:1], vcc
	global_store_dwordx4 v152, v[28:31], s[10:11] sc1
	s_or_b64 exec, exec, s[0:1]
	s_waitcnt vmcnt(7)
	v_mul_f32_e32 v146, 0x39800000, v145
	v_lshl_add_u32 v152, v137, 10, v166
	v_mov_b32_e32 v147, v146
	v_add_u32_e32 v153, 0xb0, v156
	v_pk_mul_f32 v[0:1], v[0:1], v[146:147]
	v_pk_mul_f32 v[2:3], v[2:3], v[146:147]
	v_pk_mul_f32 v[4:5], v[4:5], v[146:147]
	v_pk_mul_f32 v[6:7], v[6:7], v[146:147]
	v_cmp_gt_i32_e32 vcc, s40, v153
	v_cvt_pk_bf16_f32 v0, v0, v1
	v_cvt_pk_bf16_f32 v1, v2, v3
	v_cvt_pk_bf16_f32 v2, v4, v5
	v_cvt_pk_bf16_f32 v3, v6, v7
	s_and_saveexec_b64 s[0:1], vcc
	global_store_dwordx4 v152, v[0:3], s[10:11] sc1
	s_or_b64 exec, exec, s[0:1]
	s_lshl_b32 s0, s6, 2
	s_addk_i32 s0, 0x100
	s_add_i32 s0, s0, 0x20040
	v_mov_b32_e32 v0, s0
	ds_read_b32 v0, v0
	s_waitcnt vmcnt(0)
	v_or_b32_e32 v1, v155, v64
	v_cmp_eq_u32_e32 vcc, 0, v1
	s_waitcnt lgkmcnt(0)
	v_readfirstlane_b32 s23, v0
	s_and_saveexec_b64 s[0:1], vcc
	s_cbranch_execz .LBB0_1624
	s_mov_b64 s[6:7], exec
	v_mbcnt_lo_u32_b32 v0, s6, 0
	v_mbcnt_hi_u32_b32 v0, s7, v0
	v_cmp_eq_u32_e32 vcc, 0, v0
	s_and_b64 s[30:31], exec, vcc
	s_mov_b64 exec, s[30:31]
	s_cbranch_execz .LBB0_1624
	s_add_i32 s23, s23, s33
	s_lshl_b32 s30, s23, 6
	s_ashr_i32 s31, s30, 31
	s_lshl_b64 s[30:31], s[30:31], 2
	s_add_u32 s30, s43, s30
	s_addc_u32 s31, s44, s31
	s_bcnt1_i32_b64 s6, s[6:7]
	v_mov_b32_e32 v0, s6
	global_atomic_add v65, v0, s[30:31]
